# v20 + P11: the 16 per-row constant chunks (g_post_ffn, gate2) are loaded once per wave into registers instead of per chunk per row; removes the load->vmcnt(0) ladder in the output stage
# speedup vs baseline: 1.0228x; 1.0228x over previous
; #define P11_LOAD(y0_, y1_, x_, t_) do { _Pragma("unroll") for (int j_ = 0; j_ < 8; ++j_) { const int k_ = 4 * lane + 256 * j_; \
;         y0_[j_] = *(const v2u*)(YA + (size_t)(2 * (t_)) * D + k_); y1_[j_] = *(const v2u*)(YA + (size_t)(2 * (t_) + 1) * D + k_); x_[j_] = *(const v2u*)(X1 + (size_t)(t_) * D + k_); } } while (0)
; __device__ __forceinline__ void phase11(const Args& a, int lane, int wave) {
;     unsigned char* ws = a.ws;
;     const float* MODF = (const float*)(ws + WS_MODF); const bf16* X1 = (const bf16*)(ws + WS_X1); const bf16* YA = (const bf16*)(ws + WS_YA); const float* g = a.in[I_GPOSTFFN];
;     const int gw = blockIdx.x * NWAVES + wave, NGW = gridDim.x * NWAVES;
;     v2u ya0[8], ya1[8], yb0[8], yb1[8], xa[8], xb[8];
;     ...
;     int t = gw;
;     if (t < T) P11_LOAD(ya0, ya1, xa, t);
.LBB0_1337:
	s_cmp_lt_i32 s92, 12
	s_cselect_b64 s[0:1], -1, 0
	s_and_b64 s[0:1], s[0:1], s[4:5]
	s_andn2_b64 vcc, exec, s[0:1]
	s_cbranch_vccnz .LBB0_1347
	s_lshl_b32 s0, s74, 3
	s_add_i32 s4, s94, s0
	s_cmpk_gt_i32 s4, 0x1fff
	s_cbranch_scc1 .LBB0_1347
	s_waitcnt lgkmcnt(0)
	s_load_dword s14, s[96:97], 0xc8
	s_add_u32 s0, s58, 0x14800000
	s_addc_u32 s1, s59, 0
	s_add_u32 s6, s58, 0x18800000
	s_addc_u32 s7, s59, 0
	s_lshl_b32 s2, s4, 1
	s_ashr_i32 s3, s2, 31
	s_waitcnt lgkmcnt(0)
	s_lshl_b32 s8, s14, 3
	s_lshl_b64 s[10:11], s[2:3], 12
	s_add_u32 s10, s6, s10
	s_addc_u32 s11, s7, s11
	s_or_b32 s2, s2, 1
	s_ashr_i32 s3, s2, 31
	s_lshl_b64 s[2:3], s[2:3], 12
	s_add_u32 s2, s6, s2
	s_addc_u32 s3, s7, s3
	s_ashr_i32 s5, s4, 31
	s_lshl_b64 s[12:13], s[4:5], 12
	s_add_u32 s12, s0, s12
	s_waitcnt vmcnt(0)
	v_lshlrev_b32_e32 v78, 3, v175
	s_addc_u32 s13, s1, s13
	global_load_dwordx2 v[2:3], v78, s[10:11]
	global_load_dwordx2 v[4:5], v78, s[10:11] offset:512
	global_load_dwordx2 v[6:7], v78, s[10:11] offset:1024
	global_load_dwordx2 v[8:9], v78, s[10:11] offset:1536
	global_load_dwordx2 v[10:11], v78, s[2:3]
	global_load_dwordx2 v[12:13], v78, s[2:3] offset:512
	global_load_dwordx2 v[14:15], v78, s[2:3] offset:1024
	global_load_dwordx2 v[16:17], v78, s[2:3] offset:1536
	global_load_dwordx2 v[18:19], v78, s[12:13]
	global_load_dwordx2 v[20:21], v78, s[12:13] offset:512
	global_load_dwordx2 v[22:23], v78, s[12:13] offset:1024
	global_load_dwordx2 v[24:25], v78, s[12:13] offset:1536
	global_load_dwordx2 v[26:27], v78, s[10:11] offset:2048
	global_load_dwordx2 v[28:29], v78, s[10:11] offset:2560
	global_load_dwordx2 v[30:31], v78, s[10:11] offset:3072
	global_load_dwordx2 v[32:33], v78, s[10:11] offset:3584
	global_load_dwordx2 v[34:35], v78, s[2:3] offset:2048
	global_load_dwordx2 v[36:37], v78, s[2:3] offset:2560
	global_load_dwordx2 v[40:41], v78, s[2:3] offset:3072
	global_load_dwordx2 v[44:45], v78, s[2:3] offset:3584
	global_load_dwordx2 v[46:47], v78, s[12:13] offset:2048
	global_load_dwordx2 v[50:51], v78, s[12:13] offset:2560
	global_load_dwordx2 v[52:53], v78, s[12:13] offset:3072
	global_load_dwordx2 v[56:57], v78, s[12:13] offset:3584
	v_mbcnt_lo_u32_b32 v1, -1, 0
	v_mbcnt_hi_u32_b32 v38, -1, v1
	v_and_b32_e32 v1, 64, v38
	v_add_u32_e32 v39, 64, v1
	v_xor_b32_e32 v1, 1, v38
	v_cmp_lt_i32_e32 vcc, v1, v39
	v_xor_b32_e32 v42, 2, v38
	v_lshlrev_b32_e32 v0, 2, v175
	v_cndmask_b32_e32 v1, v38, v1, vcc
	v_cmp_lt_i32_e32 vcc, v42, v39
	v_mov_b32_e32 v79, 0
	s_add_u32 s2, s58, 0x30a000
	v_cndmask_b32_e32 v42, v38, v42, vcc
	v_lshlrev_b32_e32 v162, 2, v42
	v_xor_b32_e32 v42, 4, v38
	v_cmp_lt_i32_e32 vcc, v42, v39
	v_lshlrev_b32_e32 v58, 4, v175
	v_or_b32_e32 v80, 0x400, v0
	v_cndmask_b32_e32 v42, v38, v42, vcc
	v_lshlrev_b32_e32 v163, 2, v42
	v_xor_b32_e32 v42, 8, v38
	v_cmp_lt_i32_e32 vcc, v42, v39
	v_or_b32_e32 v82, 0x500, v0
	v_or_b32_e32 v84, 0x600, v0
	v_cndmask_b32_e32 v42, v38, v42, vcc
	v_lshlrev_b32_e32 v164, 2, v42
	v_xor_b32_e32 v42, 16, v38
	v_cmp_lt_i32_e32 vcc, v42, v39
	v_or_b32_e32 v86, 0x700, v0
	s_addc_u32 s3, s59, 0
	v_cndmask_b32_e32 v42, v38, v42, vcc
	v_lshlrev_b32_e32 v165, 2, v42
	v_xor_b32_e32 v42, 32, v38
	v_cmp_lt_i32_e32 vcc, v42, v39
	v_mov_b32_e32 v59, v79
	v_or_b32_e32 v48, 0x400, v58
	v_cndmask_b32_e32 v38, v38, v42, vcc
	v_lshlrev_b32_e32 v166, 2, v38
	v_lshl_add_u64 v[38:39], s[26:27], 0, v[58:59]
	v_lshl_add_u64 v[42:43], s[2:3], 0, v[58:59]
	v_mov_b32_e32 v49, v79
	v_or_b32_e32 v54, 0x800, v58
	v_mov_b32_e32 v55, v79
	v_or_b32_e32 v58, 0xc00, v58
	v_lshlrev_b32_e32 v62, 2, v80
	v_mov_b32_e32 v63, v79
	v_lshlrev_b32_e32 v66, 2, v82
	v_mov_b32_e32 v67, v79
	v_lshlrev_b32_e32 v70, 2, v84
	v_mov_b32_e32 v71, v79
	v_lshlrev_b32_e32 v74, 2, v86
	v_mov_b32_e32 v75, v79
	v_lshl_add_u64 v[76:77], s[6:7], 0, v[78:79]
	v_lshl_add_u64 v[78:79], s[0:1], 0, v[78:79]
	s_lshl_b32 s9, s14, 4
	s_lshl_b32 s11, s14, 5
	s_lshl_b32 s0, s94, 1
	v_lshlrev_b32_e32 v1, 2, v1
	v_lshl_add_u64 v[48:49], s[2:3], 0, v[48:49]
	v_lshl_add_u64 v[54:55], s[2:3], 0, v[54:55]
	v_lshl_add_u64 v[58:59], s[2:3], 0, v[58:59]
	v_lshl_add_u64 v[60:61], s[26:27], 0, v[62:63]
	v_lshl_add_u64 v[62:63], s[2:3], 0, v[62:63]
	v_lshl_add_u64 v[64:65], s[26:27], 0, v[66:67]
	v_lshl_add_u64 v[66:67], s[2:3], 0, v[66:67]
	v_lshl_add_u64 v[68:69], s[26:27], 0, v[70:71]
	v_lshl_add_u64 v[70:71], s[2:3], 0, v[70:71]
	v_lshl_add_u64 v[72:73], s[26:27], 0, v[74:75]
	v_lshl_add_u64 v[74:75], s[2:3], 0, v[74:75]
	s_lshl_b32 s10, s74, 4
	s_add_i32 s12, s11, s0
	s_add_i32 s13, s9, s0
	v_mov_b32_e32 v167, 0x358637bd
	s_mov_b32 s14, 0xf800000
	v_mov_b32_e32 v168, 0x260
	v_lshlrev_b32_e32 v169, 2, v80
	v_lshlrev_b32_e32 v170, 2, v82
	v_lshlrev_b32_e32 v171, 2, v84
	v_lshlrev_b32_e32 v172, 2, v86
	global_load_dwordx4 v[192:195], v[60:61], off
	global_load_dwordx4 v[196:199], v[62:63], off
	global_load_dwordx4 v[200:203], v[64:65], off
	global_load_dwordx4 v[204:207], v[66:67], off
	global_load_dwordx4 v[208:211], v[68:69], off
	global_load_dwordx4 v[212:215], v[70:71], off
	global_load_dwordx4 v[216:219], v[72:73], off
	global_load_dwordx4 v[220:223], v[74:75], off
	global_load_dwordx4 v[224:227], v[38:39], off
	global_load_dwordx4 v[228:231], v[38:39], off offset:1024
	global_load_dwordx4 v[232:235], v[38:39], off offset:2048
	global_load_dwordx4 v[236:239], v[38:39], off offset:3072
	global_load_dwordx4 v[240:243], v[42:43], off
	global_load_dwordx4 v[60:63], v[48:49], off
	global_load_dwordx4 v[64:67], v[54:55], off
	global_load_dwordx4 v[68:71], v[58:59], off
	s_branch .LBB0_1342
.Lp11_skip:
	s_waitcnt vmcnt(0)
	s_branch .LBB0_1344
.LBB0_1340:
	v_lshlrev_b32_e32 v128, 16, v80
	v_and_b32_e32 v129, 0xffff0000, v80
	v_lshlrev_b32_e32 v130, 16, v100
	v_and_b32_e32 v131, 0xffff0000, v100
	v_pk_add_f32 v[132:133], v[128:129], v[130:131]
	v_lshlrev_b32_e32 v128, 16, v81
	v_and_b32_e32 v129, 0xffff0000, v81
	v_lshlrev_b32_e32 v130, 16, v101
	v_and_b32_e32 v131, 0xffff0000, v101
	v_pk_add_f32 v[142:143], v[128:129], v[130:131]
	v_lshlrev_b32_e32 v128, 16, v82
	v_and_b32_e32 v129, 0xffff0000, v82
	v_lshlrev_b32_e32 v130, 16, v98
	v_and_b32_e32 v131, 0xffff0000, v98
	v_pk_add_f32 v[128:129], v[128:129], v[130:131]
	v_lshlrev_b32_e32 v130, 16, v83
	v_and_b32_e32 v131, 0xffff0000, v83
	v_lshlrev_b32_e32 v134, 16, v99
	v_and_b32_e32 v135, 0xffff0000, v99
	v_pk_add_f32 v[130:131], v[130:131], v[134:135]
	v_mov_b32_e32 v136, v129
	v_mov_b32_e32 v137, v133
	v_mov_b32_e32 v134, v128
	v_mov_b32_e32 v135, v132
	v_pk_mul_f32 v[136:137], v[136:137], v[136:137]
	v_mov_b32_e32 v138, v131
	v_mov_b32_e32 v139, v143
	v_pk_fma_f32 v[134:135], v[134:135], v[134:135], v[136:137]
	v_mov_b32_e32 v136, v130
	v_mov_b32_e32 v137, v142
	v_pk_mul_f32 v[138:139], v[138:139], v[138:139]
	v_lshlrev_b32_e32 v144, 16, v95
	v_pk_fma_f32 v[136:137], v[136:137], v[136:137], v[138:139]
	v_lshlrev_b32_e32 v138, 16, v97
	v_pk_add_f32 v[134:135], v[134:135], v[136:137]
	v_lshlrev_b32_e32 v136, 16, v96
	v_pk_add_f32 v[148:149], v[134:135], v[134:135] op_sel_hi:[0,1]
	v_lshlrev_b32_e32 v134, 16, v84
	v_and_b32_e32 v135, 0xffff0000, v84
	v_and_b32_e32 v137, 0xffff0000, v96
	v_pk_add_f32 v[134:135], v[134:135], v[136:137]
	v_lshlrev_b32_e32 v136, 16, v85
	v_and_b32_e32 v137, 0xffff0000, v85
	v_and_b32_e32 v139, 0xffff0000, v97
	v_pk_add_f32 v[140:141], v[136:137], v[138:139]
	v_mov_b32_e32 v138, v135
	v_mov_b32_e32 v139, v141
	v_mov_b32_e32 v136, v134
	v_mov_b32_e32 v137, v140
	v_pk_mul_f32 v[138:139], v[138:139], v[138:139]
	v_and_b32_e32 v145, 0xffff0000, v95
	v_pk_fma_f32 v[136:137], v[136:137], v[136:137], v[138:139]
	v_lshlrev_b32_e32 v138, 16, v94
	v_pk_add_f32 v[150:151], v[136:137], v[136:137] op_sel_hi:[0,1]
	v_lshlrev_b32_e32 v136, 16, v86
	v_and_b32_e32 v137, 0xffff0000, v86
	v_and_b32_e32 v139, 0xffff0000, v94
	v_pk_add_f32 v[138:139], v[136:137], v[138:139]
	v_lshlrev_b32_e32 v136, 16, v87
	v_and_b32_e32 v137, 0xffff0000, v87
	v_pk_add_f32 v[146:147], v[136:137], v[144:145]
	v_mul_f32_e32 v136, v138, v138
	v_pk_fma_f32 v[152:153], v[138:139], v[138:139], v[136:137] op_sel_hi:[1,1,0]
	v_mul_f32_e32 v136, v146, v146
	v_pk_fma_f32 v[154:155], v[146:147], v[146:147], v[136:137] op_sel_hi:[1,1,0]
	v_lshlrev_b32_e32 v136, 16, v88
	v_and_b32_e32 v137, 0xffff0000, v88
	v_lshlrev_b32_e32 v144, 16, v110
	v_and_b32_e32 v145, 0xffff0000, v110
	v_pk_add_f32 v[136:137], v[136:137], v[144:145]
	v_lshlrev_b32_e32 v144, 16, v89
	v_and_b32_e32 v145, 0xffff0000, v89
	v_lshlrev_b32_e32 v156, 16, v111
	v_and_b32_e32 v157, 0xffff0000, v111
	v_pk_add_f32 v[144:145], v[144:145], v[156:157]
	v_pk_mul_f32 v[156:157], v[136:137], v[136:137]
	v_pk_mul_f32 v[158:159], v[144:145], v[144:145]
	v_mov_b32_e32 v152, v156
	v_mov_b32_e32 v154, v157
	v_mov_b32_e32 v150, v158
	v_mov_b32_e32 v148, v159
	v_pk_add_f32 v[152:153], v[152:153], v[154:155]
	v_pk_add_f32 v[148:149], v[150:151], v[148:149]
	v_lshlrev_b32_e32 v150, 16, v108
	v_pk_add_f32 v[148:149], v[152:153], v[148:149]
	v_and_b32_e32 v151, 0xffff0000, v108
	v_pk_add_f32 v[174:175], v[148:149], v[148:149] op_sel_hi:[0,1]
	v_lshlrev_b32_e32 v148, 16, v90
	v_and_b32_e32 v149, 0xffff0000, v90
	v_pk_add_f32 v[148:149], v[148:149], v[150:151]
	v_lshlrev_b32_e32 v150, 16, v91
	v_and_b32_e32 v151, 0xffff0000, v91
	v_lshlrev_b32_e32 v152, 16, v109
	v_and_b32_e32 v153, 0xffff0000, v109
	v_pk_add_f32 v[154:155], v[150:151], v[152:153]
	v_mov_b32_e32 v152, v149
	v_mov_b32_e32 v153, v155
	v_mov_b32_e32 v150, v148
	v_mov_b32_e32 v151, v154
	v_pk_mul_f32 v[152:153], v[152:153], v[152:153]
	v_lshlrev_b32_e32 v156, 16, v107
	v_pk_fma_f32 v[150:151], v[150:151], v[150:151], v[152:153]
	v_lshlrev_b32_e32 v152, 16, v106
	v_pk_add_f32 v[176:177], v[150:151], v[150:151] op_sel_hi:[0,1]
	v_lshlrev_b32_e32 v150, 16, v92
	v_and_b32_e32 v151, 0xffff0000, v92
	v_and_b32_e32 v153, 0xffff0000, v106
	v_pk_add_f32 v[152:153], v[150:151], v[152:153]
	v_lshlrev_b32_e32 v150, 16, v93
	v_and_b32_e32 v151, 0xffff0000, v93
	v_and_b32_e32 v157, 0xffff0000, v107
	v_pk_add_f32 v[158:159], v[150:151], v[156:157]
	v_mul_f32_e32 v150, v152, v152
	v_pk_fma_f32 v[178:179], v[152:153], v[152:153], v[150:151] op_sel_hi:[1,1,0]
	v_mul_f32_e32 v150, v158, v158
	v_pk_fma_f32 v[180:181], v[158:159], v[158:159], v[150:151] op_sel_hi:[1,1,0]
	v_lshlrev_b32_e32 v150, 16, v102
	v_and_b32_e32 v151, 0xffff0000, v102
	v_lshlrev_b32_e32 v156, 16, v104
	v_and_b32_e32 v157, 0xffff0000, v104
	v_pk_add_f32 v[150:151], v[150:151], v[156:157]
	v_lshlrev_b32_e32 v156, 16, v103
	v_and_b32_e32 v157, 0xffff0000, v103
	v_lshlrev_b32_e32 v182, 16, v105
	v_and_b32_e32 v183, 0xffff0000, v105
	v_pk_add_f32 v[156:157], v[156:157], v[182:183]
	v_pk_mul_f32 v[182:183], v[150:151], v[150:151]
	v_pk_mul_f32 v[184:185], v[156:157], v[156:157]
	v_mov_b32_e32 v178, v182
	v_mov_b32_e32 v180, v183
	v_mov_b32_e32 v176, v184
	v_mov_b32_e32 v174, v185
	v_pk_add_f32 v[178:179], v[178:179], v[180:181]
	v_pk_add_f32 v[174:175], v[176:177], v[174:175]
	s_ashr_i32 s3, s2, 31
	v_pk_add_f32 v[174:175], v[178:179], v[174:175]
	v_lshlrev_b32_e32 v186, 16, v119
	v_add_f32_e32 v161, v174, v175
	ds_bpermute_b32 v173, v1, v161
	v_and_b32_e32 v187, 0xffff0000, v119
	s_waitcnt lgkmcnt(0)
	v_add_f32_e32 v161, v161, v173
	ds_bpermute_b32 v173, v162, v161
	s_waitcnt lgkmcnt(0)
	v_add_f32_e32 v161, v161, v173
	ds_bpermute_b32 v173, v163, v161
	s_waitcnt lgkmcnt(0)
	v_add_f32_e32 v161, v161, v173
	ds_bpermute_b32 v173, v164, v161
	s_waitcnt lgkmcnt(0)
	v_add_f32_e32 v161, v161, v173
	ds_bpermute_b32 v173, v165, v161
	s_waitcnt lgkmcnt(0)
	v_add_f32_e32 v161, v161, v173
	ds_bpermute_b32 v173, v166, v161
	s_waitcnt lgkmcnt(0)
	v_add_f32_e32 v161, v161, v173
	v_fmamk_f32 v161, v161, 0x3a000000, v167
	v_mul_f32_e32 v173, 0x4f800000, v161
	v_cmp_gt_f32_e32 vcc, s14, v161
	s_nop 1
	v_cndmask_b32_e32 v161, v161, v173, vcc
	v_sqrt_f32_e32 v173, v161
	s_nop 0
	v_add_u32_e32 v182, -1, v173
	v_fma_f32 v183, -v182, v173, v161
	v_cmp_ge_f32_e64 s[0:1], 0, v183
	v_add_u32_e32 v183, 1, v173
	s_nop 0
	v_cndmask_b32_e64 v182, v173, v182, s[0:1]
	v_fma_f32 v173, -v183, v173, v161
	v_cmp_lt_f32_e64 s[0:1], 0, v173
	s_nop 1
	v_cndmask_b32_e64 v173, v182, v183, s[0:1]
	v_mul_f32_e32 v182, 0x37800000, v173
	v_cndmask_b32_e32 v173, v173, v182, vcc
	v_cmp_class_f32_e32 vcc, v161, v168
	s_nop 1
	v_cndmask_b32_e32 v161, v173, v161, vcc
	v_div_scale_f32 v173, s[0:1], v161, v161, 1.0
	v_rcp_f32_e32 v182, v173
	s_lshl_b64 s[0:1], s[2:3], 13
	s_add_u32 s0, s56, s0
	s_addc_u32 s1, s57, s1
	v_fma_f32 v183, -v173, v182, 1.0
	v_fmac_f32_e32 v182, v183, v182
	v_div_scale_f32 v183, vcc, 1.0, v161, 1.0
	v_mul_f32_e32 v184, v183, v182
	v_fma_f32 v185, -v173, v184, v183
	v_fmac_f32_e32 v184, v185, v182
	v_fma_f32 v173, -v173, v184, v183
	v_div_fmas_f32 v173, v173, v182, v184
	v_div_fixup_f32 v182, v173, v161, 1.0
	v_pk_mul_f32 v[142:143], v[142:143], v[182:183] op_sel_hi:[1,0]
	v_pk_mul_f32 v[132:133], v[132:133], v[182:183] op_sel_hi:[1,0]
	v_lshlrev_b32_e32 v184, 16, v118
	v_and_b32_e32 v185, 0xffff0000, v118
	v_pk_mul_f32 v[132:133], v[224:225], v[132:133]
	v_pk_mul_f32 v[142:143], v[226:227], v[142:143]
	v_pk_fma_f32 v[174:175], v[240:241], v[132:133], v[184:185]
	v_pk_fma_f32 v[176:177], v[242:243], v[142:143], v[186:187]
	global_store_dwordx4 v160, v[174:177], s[0:1]
	s_nop 1
	s_nop 0
	v_pk_mul_f32 v[128:129], v[128:129], v[182:183] op_sel_hi:[1,0]
	v_pk_mul_f32 v[130:131], v[130:131], v[182:183] op_sel_hi:[1,0]
	v_lshlrev_b32_e32 v132, 16, v116
	v_and_b32_e32 v133, 0xffff0000, v116
	v_lshlrev_b32_e32 v142, 16, v117
	v_and_b32_e32 v143, 0xffff0000, v117
	v_pk_mul_f32 v[134:135], v[134:135], v[182:183] op_sel_hi:[1,0]
	v_pk_mul_f32 v[140:141], v[140:141], v[182:183] op_sel_hi:[1,0]
	v_pk_mul_f32 v[138:139], v[138:139], v[182:183] op_sel_hi:[1,0]
	v_pk_mul_f32 v[146:147], v[146:147], v[182:183] op_sel_hi:[1,0]
	v_pk_mul_f32 v[136:137], v[136:137], v[182:183] op_sel_hi:[1,0]
	v_pk_mul_f32 v[130:131], v[230:231], v[130:131]
	v_pk_mul_f32 v[128:129], v[228:229], v[128:129]
	v_pk_fma_f32 v[130:131], v[62:63], v[130:131], v[142:143]
	v_pk_fma_f32 v[128:129], v[60:61], v[128:129], v[132:133]
	global_store_dwordx4 v160, v[128:131], s[0:1] offset:1024
	s_nop 1
	s_nop 0
	v_lshlrev_b32_e32 v132, 16, v114
	v_and_b32_e32 v133, 0xffff0000, v114
	v_lshlrev_b32_e32 v142, 16, v115
	v_and_b32_e32 v143, 0xffff0000, v115
	v_pk_mul_f32 v[130:131], v[234:235], v[140:141]
	v_pk_mul_f32 v[128:129], v[232:233], v[134:135]
	v_pk_fma_f32 v[130:131], v[66:67], v[130:131], v[142:143]
	v_pk_fma_f32 v[128:129], v[64:65], v[128:129], v[132:133]
	global_store_dwordx4 v160, v[128:131], s[0:1] offset:2048
	s_nop 1
	s_nop 0
	v_lshlrev_b32_e32 v140, 16, v112
	v_and_b32_e32 v141, 0xffff0000, v112
	v_lshlrev_b32_e32 v142, 16, v113
	v_and_b32_e32 v143, 0xffff0000, v113
	v_pk_mul_f32 v[130:131], v[146:147], v[238:239]
	v_pk_mul_f32 v[128:129], v[138:139], v[236:237]
	v_pk_fma_f32 v[130:131], v[70:71], v[130:131], v[142:143]
	v_pk_fma_f32 v[128:129], v[68:69], v[128:129], v[140:141]
	global_store_dwordx4 v160, v[128:131], s[0:1] offset:3072
	s_nop 1
	s_nop 0
	v_pk_mul_f32 v[142:143], v[144:145], v[182:183] op_sel_hi:[1,0]
	v_lshlrev_b32_e32 v138, 16, v126
	v_and_b32_e32 v139, 0xffff0000, v126
	v_lshlrev_b32_e32 v140, 16, v127
	v_and_b32_e32 v141, 0xffff0000, v127
	v_pk_mul_f32 v[130:131], v[142:143], v[194:195]
	v_pk_mul_f32 v[128:129], v[136:137], v[192:193]
	v_pk_fma_f32 v[130:131], v[198:199], v[130:131], v[140:141]
	v_pk_fma_f32 v[128:129], v[196:197], v[128:129], v[138:139]
	global_store_dwordx4 v169, v[128:131], s[0:1]
	s_nop 1
	s_nop 0
	v_pk_mul_f32 v[140:141], v[148:149], v[182:183] op_sel_hi:[1,0]
	v_pk_mul_f32 v[142:143], v[154:155], v[182:183] op_sel_hi:[1,0]
	v_lshlrev_b32_e32 v136, 16, v124
	v_and_b32_e32 v137, 0xffff0000, v124
	v_lshlrev_b32_e32 v138, 16, v125
	v_and_b32_e32 v139, 0xffff0000, v125
	v_pk_mul_f32 v[130:131], v[142:143], v[202:203]
	v_pk_mul_f32 v[128:129], v[140:141], v[200:201]
	v_pk_fma_f32 v[130:131], v[206:207], v[130:131], v[138:139]
	v_pk_fma_f32 v[128:129], v[204:205], v[128:129], v[136:137]
	global_store_dwordx4 v170, v[128:131], s[0:1]
	s_nop 1
	s_nop 0
	v_pk_mul_f32 v[140:141], v[152:153], v[182:183] op_sel_hi:[1,0]
	v_pk_mul_f32 v[142:143], v[158:159], v[182:183] op_sel_hi:[1,0]
	v_lshlrev_b32_e32 v136, 16, v122
	v_and_b32_e32 v137, 0xffff0000, v122
	v_lshlrev_b32_e32 v138, 16, v123
	v_and_b32_e32 v139, 0xffff0000, v123
	v_pk_mul_f32 v[130:131], v[142:143], v[210:211]
	v_pk_mul_f32 v[128:129], v[140:141], v[208:209]
	v_pk_fma_f32 v[130:131], v[214:215], v[130:131], v[138:139]
	v_pk_fma_f32 v[128:129], v[212:213], v[128:129], v[136:137]
	global_store_dwordx4 v171, v[128:131], s[0:1]
	s_nop 1
	s_nop 0
	v_pk_mul_f32 v[140:141], v[150:151], v[182:183] op_sel_hi:[1,0]
	v_pk_mul_f32 v[142:143], v[156:157], v[182:183] op_sel_hi:[1,0]
	v_lshlrev_b32_e32 v136, 16, v120
	v_and_b32_e32 v137, 0xffff0000, v120
	v_lshlrev_b32_e32 v138, 16, v121
	v_and_b32_e32 v139, 0xffff0000, v121
	v_pk_mul_f32 v[130:131], v[142:143], v[218:219]
	v_pk_mul_f32 v[128:129], v[140:141], v[216:217]
	v_pk_fma_f32 v[130:131], v[222:223], v[130:131], v[138:139]
	v_pk_fma_f32 v[128:129], v[220:221], v[128:129], v[136:137]
	global_store_dwordx4 v172, v[128:131], s[0:1]
	s_nop 1

.LBB0_1344:
	s_waitcnt vmcnt(22)
	v_lshlrev_b32_e32 v132, 16, v4
	v_and_b32_e32 v133, 0xffff0000, v4
	s_waitcnt vmcnt(18)
	v_lshlrev_b32_e32 v134, 16, v12
	v_and_b32_e32 v135, 0xffff0000, v12
	v_lshlrev_b32_e32 v128, 16, v2
	v_and_b32_e32 v129, 0xffff0000, v2
	v_lshlrev_b32_e32 v130, 16, v10
	v_and_b32_e32 v131, 0xffff0000, v10
	v_pk_add_f32 v[142:143], v[134:135], v[132:133]
	v_lshlrev_b32_e32 v134, 16, v5
	v_and_b32_e32 v135, 0xffff0000, v5
	v_lshlrev_b32_e32 v136, 16, v13
	v_and_b32_e32 v137, 0xffff0000, v13
	v_pk_add_f32 v[150:151], v[130:131], v[128:129]
	v_lshlrev_b32_e32 v128, 16, v3
	v_and_b32_e32 v129, 0xffff0000, v3
	v_lshlrev_b32_e32 v130, 16, v11
	v_and_b32_e32 v131, 0xffff0000, v11
	v_pk_add_f32 v[158:159], v[136:137], v[134:135]
	v_lshlrev_b32_e32 v136, 16, v6
	s_waitcnt vmcnt(17)
	v_lshlrev_b32_e32 v138, 16, v14
	v_and_b32_e32 v137, 0xffff0000, v6
	v_and_b32_e32 v139, 0xffff0000, v14
	v_pk_add_f32 v[160:161], v[130:131], v[128:129]
	v_mul_f32_e32 v132, v143, v143
	v_mul_f32_e32 v134, v159, v159
	v_pk_add_f32 v[140:141], v[138:139], v[136:137]
	v_lshlrev_b32_e32 v136, 16, v7
	v_lshlrev_b32_e32 v138, 16, v15
	v_and_b32_e32 v137, 0xffff0000, v7
	v_and_b32_e32 v139, 0xffff0000, v15
	v_pk_mul_f32 v[130:131], v[160:161], v[160:161]
	v_pk_fma_f32 v[132:133], v[142:143], v[142:143], v[132:133] op_sel_hi:[1,1,0]
	v_pk_fma_f32 v[134:135], v[158:159], v[158:159], v[134:135] op_sel_hi:[1,1,0]
	v_pk_add_f32 v[152:153], v[138:139], v[136:137]
	v_pk_mul_f32 v[136:137], v[140:141], v[140:141]
	v_mul_f32_e32 v128, v151, v151
	v_mov_b32_e32 v135, v136
	v_mov_b32_e32 v133, v137
	v_pk_mov_b32 v[130:131], v[130:131], v[152:153] op_sel:[1,0]
	v_pk_fma_f32 v[128:129], v[150:151], v[150:151], v[128:129] op_sel_hi:[1,1,0]
	v_pk_mul_f32 v[138:139], v[152:153], v[152:153]
	v_pk_add_f32 v[132:133], v[134:135], v[132:133]
	v_pk_fma_f32 v[134:135], v[160:161], v[160:161], v[130:131]
	v_pk_mul_f32 v[130:131], v[152:153], v[130:131] op_sel_hi:[0,1]
	v_mov_b32_e32 v135, v131
	v_mov_b32_e32 v129, v139
	v_pk_add_f32 v[128:129], v[134:135], v[128:129]
	s_waitcnt vmcnt(7)
	v_lshlrev_b32_e32 v134, 16, v34
	v_pk_add_f32 v[130:131], v[128:129], v[132:133]
	v_lshlrev_b32_e32 v129, 16, v9
	v_lshlrev_b32_e32 v128, 16, v8
	v_lshlrev_b32_e32 v133, 16, v17
	v_lshlrev_b32_e32 v132, 16, v16
	v_pk_add_f32 v[146:147], v[132:133], v[128:129]
	v_and_b32_e32 v129, 0xffff0000, v9
	v_and_b32_e32 v128, 0xffff0000, v8
	v_and_b32_e32 v133, 0xffff0000, v17
	v_and_b32_e32 v132, 0xffff0000, v16
	v_pk_add_f32 v[156:157], v[132:133], v[128:129]
	v_and_b32_e32 v135, 0xffff0000, v34
	v_pk_mul_f32 v[128:129], v[156:157], v[156:157]
	s_waitcnt vmcnt(5)
	v_lshlrev_b32_e32 v144, 16, v41
	v_pk_fma_f32 v[132:133], v[146:147], v[146:147], v[128:129]
	v_lshlrev_b32_e32 v128, 16, v26
	v_and_b32_e32 v129, 0xffff0000, v26
	v_pk_add_f32 v[138:139], v[134:135], v[128:129]
	v_lshlrev_b32_e32 v134, 16, v35
	v_mul_f32_e32 v128, v139, v139
	v_pk_fma_f32 v[174:175], v[138:139], v[138:139], v[128:129] op_sel_hi:[1,1,0]
	v_lshlrev_b32_e32 v128, 16, v27
	v_and_b32_e32 v129, 0xffff0000, v27
	v_and_b32_e32 v135, 0xffff0000, v35
	v_pk_add_f32 v[154:155], v[134:135], v[128:129]
	v_lshlrev_b32_e32 v134, 16, v36
	v_mul_f32_e32 v128, v155, v155
	v_pk_fma_f32 v[176:177], v[154:155], v[154:155], v[128:129] op_sel_hi:[1,1,0]
	v_lshlrev_b32_e32 v128, 16, v28
	v_and_b32_e32 v129, 0xffff0000, v28
	v_and_b32_e32 v135, 0xffff0000, v36
	v_pk_add_f32 v[136:137], v[134:135], v[128:129]
	v_lshlrev_b32_e32 v128, 16, v29
	v_lshlrev_b32_e32 v134, 16, v37
	v_and_b32_e32 v129, 0xffff0000, v29
	v_and_b32_e32 v135, 0xffff0000, v37
	v_pk_add_f32 v[148:149], v[134:135], v[128:129]
	v_lshlrev_b32_e32 v128, 16, v30
	v_and_b32_e32 v129, 0xffff0000, v30
	v_lshlrev_b32_e32 v134, 16, v40
	v_and_b32_e32 v135, 0xffff0000, v40
	v_pk_add_f32 v[134:135], v[134:135], v[128:129]
	v_and_b32_e32 v145, 0xffff0000, v41
	v_mul_f32_e32 v128, v135, v135
	v_pk_fma_f32 v[182:183], v[134:135], v[134:135], v[128:129] op_sel_hi:[1,1,0]
	v_lshlrev_b32_e32 v128, 16, v31
	v_and_b32_e32 v129, 0xffff0000, v31
	v_pk_add_f32 v[144:145], v[144:145], v[128:129]
	v_pk_mul_f32 v[180:181], v[148:149], v[148:149]
	v_mul_f32_e32 v128, v145, v145
	v_pk_fma_f32 v[184:185], v[144:145], v[144:145], v[128:129] op_sel_hi:[1,1,0]
	v_lshlrev_b32_e32 v128, 16, v32
	s_waitcnt vmcnt(4)
	v_lshlrev_b32_e32 v186, 16, v44
	v_and_b32_e32 v129, 0xffff0000, v32
	v_and_b32_e32 v187, 0xffff0000, v44
	v_lshlrev_b32_e32 v175, 16, v33
	v_lshlrev_b32_e32 v177, 16, v45
	v_pk_add_f32 v[130:131], v[130:131], v[130:131] op_sel:[0,1] op_sel_hi:[1,0]
	v_pk_add_f32 v[132:133], v[132:133], v[132:133] op_sel:[1,0] op_sel_hi:[0,1]
	v_pk_mul_f32 v[178:179], v[136:137], v[136:137]
	v_pk_add_f32 v[128:129], v[186:187], v[128:129]
	v_and_b32_e32 v187, 0xffff0000, v33
	v_and_b32_e32 v189, 0xffff0000, v45
	v_mov_b32_e32 v131, v177
	v_mov_b32_e32 v133, v175
	v_mov_b32_e32 v188, v180
	v_mov_b32_e32 v186, v181
	v_pk_add_f32 v[130:131], v[130:131], v[132:133]
	v_pk_add_f32 v[174:175], v[176:177], v[174:175]
	v_pk_add_f32 v[132:133], v[188:189], v[186:187]
	v_mov_b32_e32 v188, v178
	v_mov_b32_e32 v186, v179
	v_pk_add_f32 v[176:177], v[188:189], v[186:187]
	v_pk_add_f32 v[180:181], v[130:131], v[174:175]
	v_pk_mul_f32 v[174:175], v[130:131], v[174:175]
	v_pk_mul_f32 v[190:191], v[128:129], v[128:129]
	v_mov_b32_e32 v181, v175
	v_pk_add_f32 v[174:175], v[132:133], v[176:177]
	v_pk_mul_f32 v[176:177], v[132:133], v[176:177]
	v_mov_b32_e32 v185, v190
	v_mov_b32_e32 v183, v191
	v_mov_b32_e32 v175, v177
	v_pk_add_f32 v[178:179], v[184:185], v[182:183]
	v_pk_add_f32 v[174:175], v[180:181], v[174:175]
	s_ashr_i32 s5, s4, 31
	v_pk_add_f32 v[174:175], v[174:175], v[178:179]
	v_and_b32_e32 v185, 0xffff0000, v19
	v_add_f32_e32 v130, v174, v175
	ds_bpermute_b32 v132, v1, v130
	s_waitcnt lgkmcnt(0)
	v_add_f32_e32 v130, v130, v132
	ds_bpermute_b32 v132, v162, v130
	s_waitcnt lgkmcnt(0)
	v_add_f32_e32 v130, v130, v132
	ds_bpermute_b32 v132, v163, v130
	s_waitcnt lgkmcnt(0)
	v_add_f32_e32 v130, v130, v132
	ds_bpermute_b32 v132, v164, v130
	s_waitcnt lgkmcnt(0)
	v_add_f32_e32 v130, v130, v132
	ds_bpermute_b32 v132, v165, v130
	s_waitcnt lgkmcnt(0)
	v_add_f32_e32 v130, v130, v132
	ds_bpermute_b32 v132, v166, v130
	s_waitcnt lgkmcnt(0)
	v_add_f32_e32 v130, v130, v132
	v_fmamk_f32 v130, v130, 0x3a000000, v167
	v_mul_f32_e32 v132, 0x4f800000, v130
	v_cmp_gt_f32_e32 vcc, s14, v130
	s_nop 1
	v_cndmask_b32_e32 v130, v130, v132, vcc
	v_sqrt_f32_e32 v132, v130
	s_nop 0
	v_add_u32_e32 v173, -1, v132
	v_fma_f32 v182, -v173, v132, v130
	v_cmp_ge_f32_e64 s[0:1], 0, v182
	v_add_u32_e32 v182, 1, v132
	s_nop 0
	v_cndmask_b32_e64 v173, v132, v173, s[0:1]
	v_fma_f32 v132, -v182, v132, v130
	v_cmp_lt_f32_e64 s[0:1], 0, v132
	s_nop 1
	v_cndmask_b32_e64 v132, v173, v182, s[0:1]
	v_mul_f32_e32 v173, 0x37800000, v132
	v_cndmask_b32_e32 v132, v132, v173, vcc
	v_cmp_class_f32_e32 vcc, v130, v168
	s_nop 1
	v_cndmask_b32_e32 v130, v132, v130, vcc
	v_div_scale_f32 v132, s[0:1], v130, v130, 1.0
	v_rcp_f32_e32 v173, v132
	s_lshl_b64 s[0:1], s[4:5], 13
	s_add_u32 s0, s56, s0
	s_addc_u32 s1, s57, s1
	v_fma_f32 v182, -v132, v173, 1.0
	v_fmac_f32_e32 v173, v182, v173
	v_div_scale_f32 v182, vcc, 1.0, v130, 1.0
	v_mul_f32_e32 v183, v182, v173
	v_fma_f32 v184, -v132, v183, v182
	v_fmac_f32_e32 v183, v184, v173
	v_fma_f32 v132, -v132, v183, v182
	v_div_fmas_f32 v132, v132, v173, v183
	v_div_fixup_f32 v130, v132, v130, 1.0
	v_pk_mul_f32 v[160:161], v[160:161], v[130:131] op_sel_hi:[1,0]
	v_pk_mul_f32 v[150:151], v[150:151], v[130:131] op_sel_hi:[1,0]
	v_lshlrev_b32_e32 v182, 16, v18
	v_and_b32_e32 v183, 0xffff0000, v18
	v_lshlrev_b32_e32 v184, 16, v19
	v_pk_mul_f32 v[150:151], v[224:225], v[150:151]
	v_pk_mul_f32 v[160:161], v[226:227], v[160:161]
	v_pk_fma_f32 v[174:175], v[240:241], v[150:151], v[182:183]
	v_pk_fma_f32 v[176:177], v[242:243], v[160:161], v[184:185]
	v_lshlrev_b32_e32 v160, 2, v0
	global_store_dwordx4 v160, v[174:177], s[0:1]
	s_nop 1
	s_nop 0
	v_pk_mul_f32 v[142:143], v[142:143], v[130:131] op_sel_hi:[1,0]
	v_pk_mul_f32 v[158:159], v[158:159], v[130:131] op_sel_hi:[1,0]
	v_lshlrev_b32_e32 v150, 16, v20
	v_and_b32_e32 v151, 0xffff0000, v20
	v_lshlrev_b32_e32 v182, 16, v21
	v_and_b32_e32 v183, 0xffff0000, v21
	v_pk_mul_f32 v[140:141], v[140:141], v[130:131] op_sel_hi:[1,0]
	v_pk_mul_f32 v[152:153], v[152:153], v[130:131] op_sel_hi:[1,0]
	v_pk_mul_f32 v[138:139], v[138:139], v[130:131] op_sel_hi:[1,0]
	v_pk_mul_f32 v[154:155], v[154:155], v[130:131] op_sel_hi:[1,0]
	v_pk_mul_f32 v[136:137], v[136:137], v[130:131] op_sel_hi:[1,0]
	v_pk_mul_f32 v[148:149], v[148:149], v[130:131] op_sel_hi:[1,0]
	v_pk_mul_f32 v[134:135], v[134:135], v[130:131] op_sel_hi:[1,0]
	v_pk_mul_f32 v[144:145], v[144:145], v[130:131] op_sel_hi:[1,0]
	v_mov_b32_e32 v132, v131
	v_pk_mul_f32 v[128:129], v[128:129], v[130:131] op_sel_hi:[1,0]
	s_andn2_b64 vcc, exec, s[6:7]
	v_pk_mul_f32 v[158:159], v[230:231], v[158:159]
	v_pk_mul_f32 v[142:143], v[228:229], v[142:143]
	v_pk_fma_f32 v[176:177], v[62:63], v[158:159], v[182:183]
	v_pk_fma_f32 v[174:175], v[60:61], v[142:143], v[150:151]
	global_store_dwordx4 v160, v[174:177], s[0:1] offset:1024
	s_nop 1
	s_nop 0
	v_lshlrev_b32_e32 v142, 16, v22
	v_and_b32_e32 v143, 0xffff0000, v22
	v_lshlrev_b32_e32 v150, 16, v23
	v_and_b32_e32 v151, 0xffff0000, v23
	v_lshlrev_b32_e32 v158, 16, v24
	v_and_b32_e32 v159, 0xffff0000, v24
	v_pk_mul_f32 v[152:153], v[234:235], v[152:153]
	v_pk_mul_f32 v[140:141], v[232:233], v[140:141]
	v_mov_b32_e32 v176, v146
	v_pk_fma_f32 v[140:141], v[64:65], v[140:141], v[142:143]
	v_pk_fma_f32 v[142:143], v[66:67], v[152:153], v[150:151]
	global_store_dwordx4 v160, v[140:143], s[0:1] offset:2048
	s_nop 1
	s_nop 0
	v_mov_b32_e32 v177, v156
	v_mov_b32_e32 v156, v147
	v_pk_mul_f32 v[146:147], v[176:177], v[130:131] op_sel_hi:[1,0]
	v_pk_mul_f32 v[156:157], v[156:157], v[130:131] op_sel_hi:[1,0]
	v_lshlrev_b32_e32 v174, 16, v25
	v_and_b32_e32 v175, 0xffff0000, v25
	v_pk_mul_f32 v[130:131], v[132:133], v[130:131] op_sel_hi:[1,0]
	v_pk_mul_f32 v[142:143], v[156:157], v[238:239]
	v_pk_mul_f32 v[140:141], v[146:147], v[236:237]
	v_pk_fma_f32 v[142:143], v[70:71], v[142:143], v[174:175]
	v_pk_fma_f32 v[140:141], v[68:69], v[140:141], v[158:159]
	global_store_dwordx4 v160, v[140:143], s[0:1] offset:3072
	s_nop 1
	s_nop 0
	v_lshlrev_b32_e32 v146, 16, v46
	v_and_b32_e32 v147, 0xffff0000, v46
	v_lshlrev_b32_e32 v156, 16, v47
	v_and_b32_e32 v157, 0xffff0000, v47
	v_pk_mul_f32 v[142:143], v[154:155], v[194:195]
	v_pk_mul_f32 v[138:139], v[138:139], v[192:193]
	v_pk_fma_f32 v[140:141], v[198:199], v[142:143], v[156:157]
	v_pk_fma_f32 v[138:139], v[196:197], v[138:139], v[146:147]
	global_store_dwordx4 v169, v[138:141], s[0:1]
	s_nop 1
	s_nop 0
	v_lshlrev_b32_e32 v142, 16, v50
	v_and_b32_e32 v143, 0xffff0000, v50
	v_lshlrev_b32_e32 v146, 16, v51
	v_and_b32_e32 v147, 0xffff0000, v51
	v_pk_mul_f32 v[140:141], v[148:149], v[202:203]
	v_pk_mul_f32 v[136:137], v[136:137], v[200:201]
	v_pk_fma_f32 v[138:139], v[206:207], v[140:141], v[146:147]
	v_pk_fma_f32 v[136:137], v[204:205], v[136:137], v[142:143]
	global_store_dwordx4 v170, v[136:139], s[0:1]
	s_nop 1
	s_nop 0
	v_lshlrev_b32_e32 v146, 16, v52
	v_and_b32_e32 v147, 0xffff0000, v52
	v_lshlrev_b32_e32 v148, 16, v53
	v_and_b32_e32 v149, 0xffff0000, v53
	v_pk_mul_f32 v[138:139], v[144:145], v[210:211]
	v_pk_mul_f32 v[134:135], v[134:135], v[208:209]
	v_pk_fma_f32 v[136:137], v[214:215], v[138:139], v[148:149]
	v_pk_fma_f32 v[134:135], v[212:213], v[134:135], v[146:147]
	global_store_dwordx4 v171, v[134:137], s[0:1]
	s_nop 1
	s_nop 0
	v_lshlrev_b32_e32 v142, 16, v56
	v_and_b32_e32 v143, 0xffff0000, v56
	v_lshlrev_b32_e32 v144, 16, v57
	v_and_b32_e32 v145, 0xffff0000, v57
	v_pk_mul_f32 v[130:131], v[130:131], v[218:219]
	v_pk_mul_f32 v[128:129], v[128:129], v[216:217]
	v_pk_fma_f32 v[130:131], v[222:223], v[130:131], v[144:145]
	v_pk_fma_f32 v[128:129], v[220:221], v[128:129], v[142:143]
	global_store_dwordx4 v172, v[128:131], s[0:1]
	s_nop 1
	s_waitcnt vmcnt(8)
	s_cbranch_vccnz .LBB0_1341
; #define P11_LOAD(y0_, y1_, x_, t_) do { _Pragma("unroll") for (int j_ = 0; j_ < 8; ++j_) { const int k_ = 4 * lane + 256 * j_; \
;         y0_[j_] = *(const v2u*)(YA + (size_t)(2 * (t_)) * D + k_); y1_[j_] = *(const v2u*)(YA + (size_t)(2 * (t_) + 1) * D + k_); x_[j_] = *(const v2u*)(X1 + (size_t)(t_) * D + k_); } } while (0)
; __device__ __forceinline__ void phase11(const Args& a, int lane, int wave) {
;     ...
;     for (; t < T; t += 2 * NGW) {
;         const int t2 = t + NGW, t3 = t + 2 * NGW;
;         if (t2 < T) P11_LOAD(yb0, yb1, xb, t2);
;         P11_ROW(ya0, ya1, xa, t);
;         if (t2 < T) { if (t3 < T) P11_LOAD(ya0, ya1, xa, t3); P11_ROW(yb0, yb1, xb, t2); }
	s_add_i32 s0, s9, s4
	s_cmpk_gt_i32 s0, 0x1fff
	s_cbranch_scc1 .LBB0_1340
	s_add_i32 s4, s10, s12
	s_ashr_i32 s5, s4, 31
	s_lshl_b64 s[6:7], s[4:5], 12
	s_add_i32 s4, s4, 1
	s_ashr_i32 s5, s4, 31
	s_ashr_i32 s1, s0, 31
	s_lshl_b64 s[4:5], s[4:5], 12
	s_lshl_b64 s[0:1], s[0:1], 12
	v_lshl_add_u64 v[32:33], v[76:77], 0, s[6:7]
	v_lshl_add_u64 v[44:45], v[76:77], 0, s[4:5]
	v_lshl_add_u64 v[56:57], v[78:79], 0, s[0:1]
	global_load_dwordx2 v[2:3], v[32:33], off
	global_load_dwordx2 v[4:5], v[32:33], off offset:512
	global_load_dwordx2 v[6:7], v[32:33], off offset:1024
	global_load_dwordx2 v[8:9], v[32:33], off offset:1536
	global_load_dwordx2 v[10:11], v[44:45], off
	global_load_dwordx2 v[12:13], v[44:45], off offset:512
	global_load_dwordx2 v[14:15], v[44:45], off offset:1024
	global_load_dwordx2 v[16:17], v[44:45], off offset:1536
	global_load_dwordx2 v[18:19], v[56:57], off
	global_load_dwordx2 v[20:21], v[56:57], off offset:512
	global_load_dwordx2 v[22:23], v[56:57], off offset:1024
	global_load_dwordx2 v[24:25], v[56:57], off offset:1536
	global_load_dwordx2 v[26:27], v[32:33], off offset:2048
	global_load_dwordx2 v[28:29], v[32:33], off offset:2560
	global_load_dwordx2 v[30:31], v[32:33], off offset:3072
	s_nop 0
	global_load_dwordx2 v[32:33], v[32:33], off offset:3584
	s_nop 0
	global_load_dwordx2 v[34:35], v[44:45], off offset:2048
	global_load_dwordx2 v[36:37], v[44:45], off offset:2560
	global_load_dwordx2 v[40:41], v[44:45], off offset:3072
	s_nop 0
	global_load_dwordx2 v[44:45], v[44:45], off offset:3584
	s_nop 0
	global_load_dwordx2 v[46:47], v[56:57], off offset:2048
	global_load_dwordx2 v[50:51], v[56:57], off offset:2560
	global_load_dwordx2 v[52:53], v[56:57], off offset:3072
	s_nop 0
	global_load_dwordx2 v[56:57], v[56:57], off offset:3584
	s_branch .LBB0_1340
